# topic loop as direct relu in VOP2 ops only (add, max with 0, fmac); no linear-term bookkeeping
# baseline (speedup 1.0000x reference)
.LBB1_53:
	s_or_b64 exec, exec, s[2:3]
	v_add_f32_e32 v130, v130, v14
	v_or_b32_e32 v14, v212, v214
	v_add_f32_e32 v134, v134, v10
	v_add_f32_e32 v10, v110, v50
	v_add_f32_e32 v50, v98, v58
	v_add_f32_e32 v58, v90, v62
	v_add_u32_e32 v62, 0x17080, v14
	v_add_f32_e32 v131, v131, v15
	v_add_f32_e32 v132, v132, v16
	v_add_f32_e32 v133, v133, v17
	v_add_f32_e32 v82, v82, v30
	ds_read_b128 v[14:17], v62
	v_add_f32_e32 v83, v83, v31
	v_add_f32_e32 v84, v84, v32
	v_add_f32_e32 v85, v85, v33
	ds_read_b128 v[30:33], v62 offset:32
	v_add_f32_e32 v2, v142, v2
	v_add_f32_e32 v138, v138, v6
	v_add_f32_e32 v6, v126, v34
	v_add_f32_e32 v34, v122, v38
	v_add_f32_e32 v38, v118, v42
	v_add_f32_e32 v114, v114, v46
	v_add_f32_e32 v42, v106, v54
	v_add_f32_e32 v18, v102, v18
	v_add_f32_e32 v46, v94, v22
	v_add_f32_e32 v141, v141, v9
	v_add_f32_e32 v135, v135, v11
	v_add_f32_e32 v136, v136, v12
	v_add_f32_e32 v137, v137, v13
	v_add_f32_e32 v9, v129, v37
	v_add_f32_e32 v37, v125, v41
	v_add_f32_e32 v41, v121, v45
	v_add_f32_e32 v115, v115, v47
	v_add_f32_e32 v116, v116, v48
	v_add_f32_e32 v117, v117, v49
	v_add_f32_e32 v11, v111, v51
	v_add_f32_e32 v12, v112, v52
	v_add_f32_e32 v13, v113, v53
	v_add_f32_e32 v45, v109, v57
	v_add_f32_e32 v51, v99, v59
	v_add_f32_e32 v52, v100, v60
	v_add_f32_e32 v53, v101, v61
	v_add_f32_e32 v59, v91, v63
	v_add_f32_e32 v60, v92, v64
	v_add_f32_e32 v61, v93, v65
	v_add_f32_e32 v57, v86, v26
	s_waitcnt lgkmcnt(1)
	v_add_f32_e32 v2, v14, v2
	v_add_f32_e32 v6, v14, v6
	v_add_f32_e32 v10, v14, v10
	v_add_f32_e32 v14, v14, v18
	s_waitcnt lgkmcnt(0)
	v_add_f32_e32 v18, v30, v138
	v_add_f32_e32 v22, v30, v34
	v_add_f32_e32 v26, v30, v42
	v_add_f32_e32 v30, v30, v46
	ds_read_b128 v[46:49], v62 offset:64
	ds_read_b128 v[62:65], v62 offset:96
	v_add_f32_e32 v3, v143, v3
	v_add_f32_e32 v4, v144, v4
	v_add_f32_e32 v5, v145, v5
	v_add_f32_e32 v139, v139, v7
	v_add_f32_e32 v140, v140, v8
	v_add_f32_e32 v7, v127, v35
	v_add_f32_e32 v8, v128, v36
	v_add_f32_e32 v35, v123, v39
	v_add_f32_e32 v36, v124, v40
	v_add_f32_e32 v39, v119, v43
	v_add_f32_e32 v40, v120, v44
	v_add_f32_e32 v43, v107, v55
	v_add_f32_e32 v44, v108, v56
	v_add_f32_e32 v19, v103, v19
	v_add_f32_e32 v20, v104, v20
	v_add_f32_e32 v21, v105, v21
	v_add_f32_e32 v54, v95, v23
	v_add_f32_e32 v55, v96, v24
	v_add_f32_e32 v56, v97, v25
	v_add_f32_e32 v86, v87, v27
	v_add_f32_e32 v87, v88, v28
	v_add_f32_e32 v88, v89, v29
	v_add_f32_e32 v3, v15, v3
	v_add_f32_e32 v4, v16, v4
	v_add_f32_e32 v5, v17, v5
	v_add_f32_e32 v7, v15, v7
	v_add_f32_e32 v8, v16, v8
	v_add_f32_e32 v9, v17, v9
	v_add_f32_e32 v11, v15, v11
	v_add_f32_e32 v12, v16, v12
	v_add_f32_e32 v13, v17, v13
	v_add_f32_e32 v15, v15, v19
	v_add_f32_e32 v16, v16, v20
	v_add_f32_e32 v17, v17, v21
	v_add_f32_e32 v19, v31, v139
	v_add_f32_e32 v20, v32, v140
	v_add_f32_e32 v21, v33, v141
	v_add_f32_e32 v23, v31, v35
	v_add_f32_e32 v24, v32, v36
	v_add_f32_e32 v25, v33, v37
	v_add_f32_e32 v27, v31, v43
	v_add_f32_e32 v28, v32, v44
	v_add_f32_e32 v29, v33, v45
	v_add_f32_e32 v31, v31, v54
	v_add_f32_e32 v32, v32, v55
	v_add_f32_e32 v33, v33, v56
	s_waitcnt lgkmcnt(1)
	v_add_f32_e32 v34, v46, v134
	v_add_f32_e32 v38, v46, v38
	v_add_f32_e32 v42, v46, v50
	v_add_f32_e32 v43, v47, v51
	v_add_f32_e32 v44, v48, v52
	v_add_f32_e32 v45, v49, v53
	v_add_f32_e32 v46, v46, v57
	s_waitcnt lgkmcnt(0)
	v_add_f32_e32 v50, v62, v130
	v_add_f32_e32 v51, v63, v131
	v_add_f32_e32 v52, v64, v132
	v_add_f32_e32 v53, v65, v133
	v_add_f32_e32 v54, v62, v114
	v_add_f32_e32 v55, v63, v115
	v_add_f32_e32 v56, v64, v116
	v_add_f32_e32 v57, v65, v117
	v_add_f32_e32 v58, v62, v58
	v_add_f32_e32 v59, v63, v59
	v_add_f32_e32 v60, v64, v60
	v_add_f32_e32 v61, v65, v61
	v_add_f32_e32 v62, v62, v82
	v_add_f32_e32 v63, v63, v83
	v_add_f32_e32 v64, v64, v84
	v_add_f32_e32 v65, v65, v85
	s_waitcnt vmcnt(3)
	s_waitcnt vmcnt(2)
	v_add_f32_e32 v35, v47, v135
	v_add_f32_e32 v39, v47, v39
	v_add_f32_e32 v47, v47, v86
	s_waitcnt vmcnt(1)
	v_add_f32_e32 v36, v48, v136
	v_add_f32_e32 v40, v48, v40
	v_add_f32_e32 v48, v48, v87
	v_add_f32_e32 v37, v49, v137
	v_add_f32_e32 v41, v49, v41
	v_add_f32_e32 v49, v49, v88
	s_waitcnt vmcnt(0)
	v_mul_u32_u24_e32 v87, 10, v225
	v_lshlrev_b32_e32 v1, 9, v1
	v_lshlrev_b32_e32 v86, 9, v87
	v_lshl_or_b32 v1, v87, 12, v1
	v_lshlrev_b32_e32 v87, 10, v224
	v_or3_b32 v1, v87, v1, v211
	v_or3_b32 v86, v86, v212, v214
	v_add_u32_e32 v1, 0x2800, v1
	s_mov_b32 s0, 0
	v_add_u32_e32 v152, s0, v86
	ds_read_b128 v[88:91], v152
	ds_read_b128 v[92:95], v152 offset:32
	ds_read_b128 v[96:99], v152 offset:64
	ds_read_b128 v[100:103], v152 offset:96
	s_addk_i32 s0, 0x200
.Ltopic_loop:
	v_add_u32_e32 v152, s0, v86
	ds_read_b128 v[136:139], v152
	ds_read_b128 v[140:143], v152 offset:32
	ds_read_b128 v[144:147], v152 offset:64
	ds_read_b128 v[148:151], v152 offset:96
	s_addk_i32 s0, 0x200
	s_waitcnt lgkmcnt(4)
	v_add_f32_e32 v104, v2, v88
	v_add_f32_e32 v108, v6, v88
	v_add_f32_e32 v112, v10, v88
	v_add_f32_e32 v116, v14, v88
	v_add_f32_e32 v105, v3, v89
	v_add_f32_e32 v109, v7, v89
	v_add_f32_e32 v113, v11, v89
	v_add_f32_e32 v117, v15, v89
	v_add_f32_e32 v106, v4, v90
	v_add_f32_e32 v110, v8, v90
	v_add_f32_e32 v114, v12, v90
	v_add_f32_e32 v118, v16, v90
	v_add_f32_e32 v107, v5, v91
	v_add_f32_e32 v111, v9, v91
	v_add_f32_e32 v115, v13, v91
	v_add_f32_e32 v119, v17, v91
	v_max_f32_e32 v104, 0, v104
	v_max_f32_e32 v108, 0, v108
	v_max_f32_e32 v112, 0, v112
	v_max_f32_e32 v116, 0, v116
	v_max_f32_e32 v105, 0, v105
	v_max_f32_e32 v109, 0, v109
	v_max_f32_e32 v113, 0, v113
	v_max_f32_e32 v117, 0, v117
	v_max_f32_e32 v106, 0, v106
	v_max_f32_e32 v110, 0, v110
	v_max_f32_e32 v114, 0, v114
	v_max_f32_e32 v118, 0, v118
	v_max_f32_e32 v107, 0, v107
	v_max_f32_e32 v111, 0, v111
	v_max_f32_e32 v115, 0, v115
	v_max_f32_e32 v119, 0, v119
	v_mul_f32_e32 v160, v66, v104
	v_mul_f32_e32 v161, v66, v108
	v_mul_f32_e32 v162, v66, v112
	v_mul_f32_e32 v163, v66, v116
	v_fmac_f32_e32 v160, v67, v105
	v_fmac_f32_e32 v161, v67, v109
	v_fmac_f32_e32 v162, v67, v113
	v_fmac_f32_e32 v163, v67, v117
	v_fmac_f32_e32 v160, v68, v106
	v_fmac_f32_e32 v161, v68, v110
	v_fmac_f32_e32 v162, v68, v114
	v_fmac_f32_e32 v163, v68, v118
	v_fmac_f32_e32 v160, v69, v107
	v_fmac_f32_e32 v161, v69, v111
	v_fmac_f32_e32 v162, v69, v115
	v_fmac_f32_e32 v163, v69, v119
	v_add_f32_e32 v120, v18, v92
	v_add_f32_e32 v124, v22, v92
	v_add_f32_e32 v128, v26, v92
	v_add_f32_e32 v132, v30, v92
	v_add_f32_e32 v121, v19, v93
	v_add_f32_e32 v125, v23, v93
	v_add_f32_e32 v129, v27, v93
	v_add_f32_e32 v133, v31, v93
	v_add_f32_e32 v122, v20, v94
	v_add_f32_e32 v126, v24, v94
	v_add_f32_e32 v130, v28, v94
	v_add_f32_e32 v134, v32, v94
	v_add_f32_e32 v123, v21, v95
	v_add_f32_e32 v127, v25, v95
	v_add_f32_e32 v131, v29, v95
	v_add_f32_e32 v135, v33, v95
	v_max_f32_e32 v120, 0, v120
	v_max_f32_e32 v124, 0, v124
	v_max_f32_e32 v128, 0, v128
	v_max_f32_e32 v132, 0, v132
	v_max_f32_e32 v121, 0, v121
	v_max_f32_e32 v125, 0, v125
	v_max_f32_e32 v129, 0, v129
	v_max_f32_e32 v133, 0, v133
	v_max_f32_e32 v122, 0, v122
	v_max_f32_e32 v126, 0, v126
	v_max_f32_e32 v130, 0, v130
	v_max_f32_e32 v134, 0, v134
	v_max_f32_e32 v123, 0, v123
	v_max_f32_e32 v127, 0, v127
	v_max_f32_e32 v131, 0, v131
	v_max_f32_e32 v135, 0, v135
	v_fmac_f32_e32 v160, v70, v120
	v_fmac_f32_e32 v161, v70, v124
	v_fmac_f32_e32 v162, v70, v128
	v_fmac_f32_e32 v163, v70, v132
	v_fmac_f32_e32 v160, v71, v121
	v_fmac_f32_e32 v161, v71, v125
	v_fmac_f32_e32 v162, v71, v129
	v_fmac_f32_e32 v163, v71, v133
	v_fmac_f32_e32 v160, v72, v122
	v_fmac_f32_e32 v161, v72, v126
	v_fmac_f32_e32 v162, v72, v130
	v_fmac_f32_e32 v163, v72, v134
	v_fmac_f32_e32 v160, v73, v123
	v_fmac_f32_e32 v161, v73, v127
	v_fmac_f32_e32 v162, v73, v131
	v_fmac_f32_e32 v163, v73, v135
	v_add_f32_e32 v104, v34, v96
	v_add_f32_e32 v108, v38, v96
	v_add_f32_e32 v112, v42, v96
	v_add_f32_e32 v116, v46, v96
	v_add_f32_e32 v105, v35, v97
	v_add_f32_e32 v109, v39, v97
	v_add_f32_e32 v113, v43, v97
	v_add_f32_e32 v117, v47, v97
	v_add_f32_e32 v106, v36, v98
	v_add_f32_e32 v110, v40, v98
	v_add_f32_e32 v114, v44, v98
	v_add_f32_e32 v118, v48, v98
	v_add_f32_e32 v107, v37, v99
	v_add_f32_e32 v111, v41, v99
	v_add_f32_e32 v115, v45, v99
	v_add_f32_e32 v119, v49, v99
	v_max_f32_e32 v104, 0, v104
	v_max_f32_e32 v108, 0, v108
	v_max_f32_e32 v112, 0, v112
	v_max_f32_e32 v116, 0, v116
	v_max_f32_e32 v105, 0, v105
	v_max_f32_e32 v109, 0, v109
	v_max_f32_e32 v113, 0, v113
	v_max_f32_e32 v117, 0, v117
	v_max_f32_e32 v106, 0, v106
	v_max_f32_e32 v110, 0, v110
	v_max_f32_e32 v114, 0, v114
	v_max_f32_e32 v118, 0, v118
	v_max_f32_e32 v107, 0, v107
	v_max_f32_e32 v111, 0, v111
	v_max_f32_e32 v115, 0, v115
	v_max_f32_e32 v119, 0, v119
	v_fmac_f32_e32 v160, v74, v104
	v_fmac_f32_e32 v161, v74, v108
	v_fmac_f32_e32 v162, v74, v112
	v_fmac_f32_e32 v163, v74, v116
	v_fmac_f32_e32 v160, v75, v105
	v_fmac_f32_e32 v161, v75, v109
	v_fmac_f32_e32 v162, v75, v113
	v_fmac_f32_e32 v163, v75, v117
	v_fmac_f32_e32 v160, v76, v106
	v_fmac_f32_e32 v161, v76, v110
	v_fmac_f32_e32 v162, v76, v114
	v_fmac_f32_e32 v163, v76, v118
	v_fmac_f32_e32 v160, v77, v107
	v_fmac_f32_e32 v161, v77, v111
	v_fmac_f32_e32 v162, v77, v115
	v_fmac_f32_e32 v163, v77, v119
	v_add_f32_e32 v120, v50, v100
	v_add_f32_e32 v124, v54, v100
	v_add_f32_e32 v128, v58, v100
	v_add_f32_e32 v132, v62, v100
	v_add_f32_e32 v121, v51, v101
	v_add_f32_e32 v125, v55, v101
	v_add_f32_e32 v129, v59, v101
	v_add_f32_e32 v133, v63, v101
	v_add_f32_e32 v122, v52, v102
	v_add_f32_e32 v126, v56, v102
	v_add_f32_e32 v130, v60, v102
	v_add_f32_e32 v134, v64, v102
	v_add_f32_e32 v123, v53, v103
	v_add_f32_e32 v127, v57, v103
	v_add_f32_e32 v131, v61, v103
	v_add_f32_e32 v135, v65, v103
	v_max_f32_e32 v120, 0, v120
	v_max_f32_e32 v124, 0, v124
	v_max_f32_e32 v128, 0, v128
	v_max_f32_e32 v132, 0, v132
	v_max_f32_e32 v121, 0, v121
	v_max_f32_e32 v125, 0, v125
	v_max_f32_e32 v129, 0, v129
	v_max_f32_e32 v133, 0, v133
	v_max_f32_e32 v122, 0, v122
	v_max_f32_e32 v126, 0, v126
	v_max_f32_e32 v130, 0, v130
	v_max_f32_e32 v134, 0, v134
	v_max_f32_e32 v123, 0, v123
	v_max_f32_e32 v127, 0, v127
	v_max_f32_e32 v131, 0, v131
	v_max_f32_e32 v135, 0, v135
	v_fmac_f32_e32 v160, v78, v120
	v_fmac_f32_e32 v161, v78, v124
	v_fmac_f32_e32 v162, v78, v128
	v_fmac_f32_e32 v163, v78, v132
	v_fmac_f32_e32 v160, v79, v121
	v_fmac_f32_e32 v161, v79, v125
	v_fmac_f32_e32 v162, v79, v129
	v_fmac_f32_e32 v163, v79, v133
	v_fmac_f32_e32 v160, v80, v122
	v_fmac_f32_e32 v161, v80, v126
	v_fmac_f32_e32 v162, v80, v130
	v_fmac_f32_e32 v163, v80, v134
	v_fmac_f32_e32 v160, v81, v123
	v_fmac_f32_e32 v161, v81, v127
	v_fmac_f32_e32 v162, v81, v131
	v_fmac_f32_e32 v163, v81, v135
	ds_write2_b32 v1, v160, v161 offset1:32
	ds_write2_b32 v1, v162, v163 offset0:64 offset1:96
	v_add_u32_e32 v1, 0x1000, v1
	v_add_u32_e32 v152, s0, v86
	ds_read_b128 v[88:91], v152
	ds_read_b128 v[92:95], v152 offset:32
	ds_read_b128 v[96:99], v152 offset:64
	ds_read_b128 v[100:103], v152 offset:96
	s_addk_i32 s0, 0x200
	s_waitcnt lgkmcnt(4)
	v_add_f32_e32 v104, v2, v136
	v_add_f32_e32 v108, v6, v136
	v_add_f32_e32 v112, v10, v136
	v_add_f32_e32 v116, v14, v136
	v_add_f32_e32 v105, v3, v137
	v_add_f32_e32 v109, v7, v137
	v_add_f32_e32 v113, v11, v137
	v_add_f32_e32 v117, v15, v137
	v_add_f32_e32 v106, v4, v138
	v_add_f32_e32 v110, v8, v138
	v_add_f32_e32 v114, v12, v138
	v_add_f32_e32 v118, v16, v138
	v_add_f32_e32 v107, v5, v139
	v_add_f32_e32 v111, v9, v139
	v_add_f32_e32 v115, v13, v139
	v_add_f32_e32 v119, v17, v139
	v_max_f32_e32 v104, 0, v104
	v_max_f32_e32 v108, 0, v108
	v_max_f32_e32 v112, 0, v112
	v_max_f32_e32 v116, 0, v116
	v_max_f32_e32 v105, 0, v105
	v_max_f32_e32 v109, 0, v109
	v_max_f32_e32 v113, 0, v113
	v_max_f32_e32 v117, 0, v117
	v_max_f32_e32 v106, 0, v106
	v_max_f32_e32 v110, 0, v110
	v_max_f32_e32 v114, 0, v114
	v_max_f32_e32 v118, 0, v118
	v_max_f32_e32 v107, 0, v107
	v_max_f32_e32 v111, 0, v111
	v_max_f32_e32 v115, 0, v115
	v_max_f32_e32 v119, 0, v119
	v_mul_f32_e32 v160, v66, v104
	v_mul_f32_e32 v161, v66, v108
	v_mul_f32_e32 v162, v66, v112
	v_mul_f32_e32 v163, v66, v116
	v_fmac_f32_e32 v160, v67, v105
	v_fmac_f32_e32 v161, v67, v109
	v_fmac_f32_e32 v162, v67, v113
	v_fmac_f32_e32 v163, v67, v117
	v_fmac_f32_e32 v160, v68, v106
	v_fmac_f32_e32 v161, v68, v110
	v_fmac_f32_e32 v162, v68, v114
	v_fmac_f32_e32 v163, v68, v118
	v_fmac_f32_e32 v160, v69, v107
	v_fmac_f32_e32 v161, v69, v111
	v_fmac_f32_e32 v162, v69, v115
	v_fmac_f32_e32 v163, v69, v119
	v_add_f32_e32 v120, v18, v140
	v_add_f32_e32 v124, v22, v140
	v_add_f32_e32 v128, v26, v140
	v_add_f32_e32 v132, v30, v140
	v_add_f32_e32 v121, v19, v141
	v_add_f32_e32 v125, v23, v141
	v_add_f32_e32 v129, v27, v141
	v_add_f32_e32 v133, v31, v141
	v_add_f32_e32 v122, v20, v142
	v_add_f32_e32 v126, v24, v142
	v_add_f32_e32 v130, v28, v142
	v_add_f32_e32 v134, v32, v142
	v_add_f32_e32 v123, v21, v143
	v_add_f32_e32 v127, v25, v143
	v_add_f32_e32 v131, v29, v143
	v_add_f32_e32 v135, v33, v143
	v_max_f32_e32 v120, 0, v120
	v_max_f32_e32 v124, 0, v124
	v_max_f32_e32 v128, 0, v128
	v_max_f32_e32 v132, 0, v132
	v_max_f32_e32 v121, 0, v121
	v_max_f32_e32 v125, 0, v125
	v_max_f32_e32 v129, 0, v129
	v_max_f32_e32 v133, 0, v133
	v_max_f32_e32 v122, 0, v122
	v_max_f32_e32 v126, 0, v126
	v_max_f32_e32 v130, 0, v130
	v_max_f32_e32 v134, 0, v134
	v_max_f32_e32 v123, 0, v123
	v_max_f32_e32 v127, 0, v127
	v_max_f32_e32 v131, 0, v131
	v_max_f32_e32 v135, 0, v135
	v_fmac_f32_e32 v160, v70, v120
	v_fmac_f32_e32 v161, v70, v124
	v_fmac_f32_e32 v162, v70, v128
	v_fmac_f32_e32 v163, v70, v132
	v_fmac_f32_e32 v160, v71, v121
	v_fmac_f32_e32 v161, v71, v125
	v_fmac_f32_e32 v162, v71, v129
	v_fmac_f32_e32 v163, v71, v133
	v_fmac_f32_e32 v160, v72, v122
	v_fmac_f32_e32 v161, v72, v126
	v_fmac_f32_e32 v162, v72, v130
	v_fmac_f32_e32 v163, v72, v134
	v_fmac_f32_e32 v160, v73, v123
	v_fmac_f32_e32 v161, v73, v127
	v_fmac_f32_e32 v162, v73, v131
	v_fmac_f32_e32 v163, v73, v135
	v_add_f32_e32 v104, v34, v144
	v_add_f32_e32 v108, v38, v144
	v_add_f32_e32 v112, v42, v144
	v_add_f32_e32 v116, v46, v144
	v_add_f32_e32 v105, v35, v145
	v_add_f32_e32 v109, v39, v145
	v_add_f32_e32 v113, v43, v145
	v_add_f32_e32 v117, v47, v145
	v_add_f32_e32 v106, v36, v146
	v_add_f32_e32 v110, v40, v146
	v_add_f32_e32 v114, v44, v146
	v_add_f32_e32 v118, v48, v146
	v_add_f32_e32 v107, v37, v147
	v_add_f32_e32 v111, v41, v147
	v_add_f32_e32 v115, v45, v147
	v_add_f32_e32 v119, v49, v147
	v_max_f32_e32 v104, 0, v104
	v_max_f32_e32 v108, 0, v108
	v_max_f32_e32 v112, 0, v112
	v_max_f32_e32 v116, 0, v116
	v_max_f32_e32 v105, 0, v105
	v_max_f32_e32 v109, 0, v109
	v_max_f32_e32 v113, 0, v113
	v_max_f32_e32 v117, 0, v117
	v_max_f32_e32 v106, 0, v106
	v_max_f32_e32 v110, 0, v110
	v_max_f32_e32 v114, 0, v114
	v_max_f32_e32 v118, 0, v118
	v_max_f32_e32 v107, 0, v107
	v_max_f32_e32 v111, 0, v111
	v_max_f32_e32 v115, 0, v115
	v_max_f32_e32 v119, 0, v119
	v_fmac_f32_e32 v160, v74, v104
	v_fmac_f32_e32 v161, v74, v108
	v_fmac_f32_e32 v162, v74, v112
	v_fmac_f32_e32 v163, v74, v116
	v_fmac_f32_e32 v160, v75, v105
	v_fmac_f32_e32 v161, v75, v109
	v_fmac_f32_e32 v162, v75, v113
	v_fmac_f32_e32 v163, v75, v117
	v_fmac_f32_e32 v160, v76, v106
	v_fmac_f32_e32 v161, v76, v110
	v_fmac_f32_e32 v162, v76, v114
	v_fmac_f32_e32 v163, v76, v118
	v_fmac_f32_e32 v160, v77, v107
	v_fmac_f32_e32 v161, v77, v111
	v_fmac_f32_e32 v162, v77, v115
	v_fmac_f32_e32 v163, v77, v119
	v_add_f32_e32 v120, v50, v148
	v_add_f32_e32 v124, v54, v148
	v_add_f32_e32 v128, v58, v148
	v_add_f32_e32 v132, v62, v148
	v_add_f32_e32 v121, v51, v149
	v_add_f32_e32 v125, v55, v149
	v_add_f32_e32 v129, v59, v149
	v_add_f32_e32 v133, v63, v149
	v_add_f32_e32 v122, v52, v150
	v_add_f32_e32 v126, v56, v150
	v_add_f32_e32 v130, v60, v150
	v_add_f32_e32 v134, v64, v150
	v_add_f32_e32 v123, v53, v151
	v_add_f32_e32 v127, v57, v151
	v_add_f32_e32 v131, v61, v151
	v_add_f32_e32 v135, v65, v151
	v_max_f32_e32 v120, 0, v120
	v_max_f32_e32 v124, 0, v124
	v_max_f32_e32 v128, 0, v128
	v_max_f32_e32 v132, 0, v132
	v_max_f32_e32 v121, 0, v121
	v_max_f32_e32 v125, 0, v125
	v_max_f32_e32 v129, 0, v129
	v_max_f32_e32 v133, 0, v133
	v_max_f32_e32 v122, 0, v122
	v_max_f32_e32 v126, 0, v126
	v_max_f32_e32 v130, 0, v130
	v_max_f32_e32 v134, 0, v134
	v_max_f32_e32 v123, 0, v123
	v_max_f32_e32 v127, 0, v127
	v_max_f32_e32 v131, 0, v131
	v_max_f32_e32 v135, 0, v135
	v_fmac_f32_e32 v160, v78, v120
	v_fmac_f32_e32 v161, v78, v124
	v_fmac_f32_e32 v162, v78, v128
	v_fmac_f32_e32 v163, v78, v132
	v_fmac_f32_e32 v160, v79, v121
	v_fmac_f32_e32 v161, v79, v125
	v_fmac_f32_e32 v162, v79, v129
	v_fmac_f32_e32 v163, v79, v133
	v_fmac_f32_e32 v160, v80, v122
	v_fmac_f32_e32 v161, v80, v126
	v_fmac_f32_e32 v162, v80, v130
	v_fmac_f32_e32 v163, v80, v134
	v_fmac_f32_e32 v160, v81, v123
	v_fmac_f32_e32 v161, v81, v127
	v_fmac_f32_e32 v162, v81, v131
	v_fmac_f32_e32 v163, v81, v135
	ds_write2_b32 v1, v160, v161 offset1:32
	ds_write2_b32 v1, v162, v163 offset0:64 offset1:96
	v_add_u32_e32 v1, 0x1000, v1
	s_cmpk_eq_i32 s0, 0x1600
	s_cbranch_scc0 .Ltopic_loop
	v_lshl_or_b32 v1, v227, 12, v226
	s_waitcnt lgkmcnt(0)
	s_barrier
	ds_read2st64_b32 v[2:3], v1 offset0:40 offset1:42
	ds_read2st64_b32 v[4:5], v1 offset0:44 offset1:46
	ds_read2st64_b32 v[6:7], v1 offset0:48 offset1:50
	v_or_b32_e32 v13, 16, v227
	s_waitcnt lgkmcnt(2)
	v_add_f32_e32 v2, s18, v2
	v_add_f32_e32 v8, v2, v3
	ds_read2st64_b32 v[2:3], v1 offset0:52 offset1:54
	s_waitcnt lgkmcnt(2)
	v_add_f32_e32 v4, v8, v4
	v_add_f32_e32 v4, v4, v5
	s_waitcnt lgkmcnt(1)
	v_add_f32_e32 v4, v4, v6
	v_add_f32_e32 v4, v4, v7
	s_waitcnt lgkmcnt(0)
	v_add_f32_e32 v2, v4, v2
	v_add_f32_e32 v2, v2, v3
	v_mul_f32_e32 v2, 0xbfb8aa3b, v2
	v_exp_f32_e32 v2, v2
	s_nop 0
	v_add_f32_e32 v4, 1.0, v2
	v_div_scale_f32 v5, s[0:1], v4, v4, 1.0
	v_rcp_f32_e32 v6, v5
	v_div_scale_f32 v7, vcc, 1.0, v4, 1.0
	ds_read2st64_b32 v[2:3], v1 offset0:104 offset1:106
	v_fma_f32 v8, -v5, v6, 1.0
	v_fmac_f32_e32 v6, v8, v6
	v_mul_f32_e32 v8, v7, v6
	v_fma_f32 v9, -v5, v8, v7
	v_fmac_f32_e32 v8, v9, v6
	v_fma_f32 v5, -v5, v8, v7
	v_div_fmas_f32 v5, v5, v6, v8
	v_div_fixup_f32 v8, v5, v4, 1.0
	ds_read2st64_b32 v[4:5], v1 offset0:108 offset1:110
	ds_read2st64_b32 v[6:7], v1 offset0:112 offset1:114
	s_waitcnt lgkmcnt(2)
	v_add_f32_e32 v2, s18, v2
	v_add_f32_e32 v9, v2, v3
	ds_read2st64_b32 v[2:3], v1 offset0:116 offset1:118
	s_waitcnt lgkmcnt(2)
	v_add_f32_e32 v4, v9, v4
	v_add_f32_e32 v4, v4, v5
	s_waitcnt lgkmcnt(1)
	v_add_f32_e32 v4, v4, v6
	v_add_f32_e32 v4, v4, v7
	s_waitcnt lgkmcnt(0)
	v_add_f32_e32 v2, v4, v2
	v_add_f32_e32 v2, v2, v3
	v_mul_f32_e32 v2, 0xbfb8aa3b, v2
	v_exp_f32_e32 v2, v2
	v_lshlrev_b32_e32 v3, 2, v227
	v_or_b32_e32 v6, 8, v227
	v_mov_b32_e32 v7, 0x17000
	v_add_f32_e32 v10, 1.0, v2
	v_div_scale_f32 v5, s[0:1], v10, v10, 1.0
	v_rcp_f32_e32 v11, v5
	v_or_b32_e32 v4, 0x17000, v3
	v_lshl_or_b32 v12, v6, 2, v7
	v_or_b32_e32 v2, 0x17010, v3
	v_or_b32_e32 v3, 0x17030, v3
	v_lshl_or_b32 v7, v13, 2, v7
	ds_read_b32 v4, v4
	ds_read_b32 v14, v2
	ds_read_b32 v12, v12
	ds_read_b32 v15, v3
	ds_read_b32 v16, v7
	s_waitcnt lgkmcnt(4)
	v_fmaak_f32 v2, v8, v4, 0xbc23d70a
	v_max_f32_e32 v8, 0, v2
	v_fma_f32 v2, -v5, v11, 1.0
	v_fmac_f32_e32 v11, v2, v11
	v_div_scale_f32 v4, vcc, 1.0, v10, 1.0
	v_mul_f32_e32 v17, v4, v11
	v_lshl_or_b32 v18, v6, 12, v226
	ds_read2st64_b32 v[2:3], v18 offset0:40 offset1:42
	v_fma_f32 v6, -v5, v17, v4
	v_fmac_f32_e32 v17, v6, v11
	v_fma_f32 v19, -v5, v17, v4
	ds_read2st64_b32 v[4:5], v18 offset0:44 offset1:46
	ds_read2st64_b32 v[6:7], v18 offset0:48 offset1:50
	s_waitcnt lgkmcnt(2)
	v_add_f32_e32 v2, s18, v2
	v_add_f32_e32 v20, v2, v3
	ds_read2st64_b32 v[2:3], v18 offset0:52 offset1:54
	s_waitcnt lgkmcnt(2)
	v_add_f32_e32 v4, v20, v4
	v_add_f32_e32 v4, v4, v5
	s_waitcnt lgkmcnt(1)
	v_add_f32_e32 v4, v4, v6
	v_add_f32_e32 v4, v4, v7
	s_waitcnt lgkmcnt(0)
	v_add_f32_e32 v2, v4, v2
	v_add_f32_e32 v2, v2, v3
	v_mul_f32_e32 v2, 0xbfb8aa3b, v2
	v_exp_f32_e32 v2, v2
	v_div_fmas_f32 v3, v19, v11, v17
	v_div_fixup_f32 v3, v3, v10, 1.0
	v_mov_b32_e32 v9, 0xbc23d70a
	v_add_f32_e32 v10, 1.0, v2
	v_div_scale_f32 v4, s[0:1], v10, v10, 1.0
	v_rcp_f32_e32 v11, v4
	v_fmaak_f32 v2, v3, v14, 0xbc23d70a
	v_max_f32_e32 v2, 0, v2
	v_add_f32_e32 v8, v8, v2
	v_fma_f32 v2, -v4, v11, 1.0
	v_fmac_f32_e32 v11, v2, v11
	v_div_scale_f32 v5, vcc, 1.0, v10, 1.0
	v_mul_f32_e32 v14, v5, v11
	ds_read2st64_b32 v[2:3], v1 offset0:232 offset1:234
	v_fma_f32 v6, -v4, v14, v5
	v_fmac_f32_e32 v14, v6, v11
	v_fma_f32 v17, -v4, v14, v5
	ds_read2st64_b32 v[4:5], v1 offset0:236 offset1:238
	ds_read2st64_b32 v[6:7], v1 offset0:240 offset1:242
	s_waitcnt lgkmcnt(2)
	v_add_f32_e32 v2, s18, v2
	v_add_f32_e32 v18, v2, v3
	ds_read2st64_b32 v[2:3], v1 offset0:244 offset1:246
	s_waitcnt lgkmcnt(2)
	v_add_f32_e32 v1, v18, v4
	v_add_f32_e32 v1, v1, v5
	s_waitcnt lgkmcnt(1)
	v_add_f32_e32 v1, v1, v6
	v_add_f32_e32 v1, v1, v7
	s_waitcnt lgkmcnt(0)
	v_add_f32_e32 v1, v1, v2
	v_add_f32_e32 v1, v1, v3
	v_mul_f32_e32 v1, 0xbfb8aa3b, v1
	v_exp_f32_e32 v1, v1
	v_div_fmas_f32 v2, v17, v11, v14
	v_div_fixup_f32 v2, v2, v10, 1.0
	v_fmaak_f32 v2, v2, v12, 0xbc23d70a
	v_add_f32_e32 v1, 1.0, v1
	v_div_scale_f32 v4, s[0:1], v1, v1, 1.0
	v_rcp_f32_e32 v10, v4
	v_max_f32_e32 v2, 0, v2
	v_add_f32_e32 v8, v8, v2
	v_div_scale_f32 v5, vcc, 1.0, v1, 1.0
	v_fma_f32 v2, -v4, v10, 1.0
	v_fmac_f32_e32 v10, v2, v10
	v_mul_f32_e32 v11, v5, v10
	v_lshl_or_b32 v12, v13, 12, v226
	ds_read2st64_b32 v[2:3], v12 offset0:40 offset1:42
	v_fma_f32 v6, -v4, v11, v5
	v_fmac_f32_e32 v11, v6, v10
	v_fma_f32 v13, -v4, v11, v5
	ds_read2st64_b32 v[4:5], v12 offset0:44 offset1:46
	ds_read2st64_b32 v[6:7], v12 offset0:48 offset1:50
	s_waitcnt lgkmcnt(2)
	v_add_f32_e32 v2, s18, v2
	v_add_f32_e32 v14, v2, v3
	ds_read2st64_b32 v[2:3], v12 offset0:52 offset1:54
	s_waitcnt lgkmcnt(2)
	v_add_f32_e32 v4, v14, v4
	v_add_f32_e32 v4, v4, v5
	s_waitcnt lgkmcnt(1)
	v_add_f32_e32 v4, v4, v6
	v_add_f32_e32 v4, v4, v7
	s_waitcnt lgkmcnt(0)
	v_add_f32_e32 v2, v4, v2
	v_add_f32_e32 v2, v2, v3
	v_mul_f32_e32 v2, 0xbfb8aa3b, v2
	v_exp_f32_e32 v2, v2
	v_div_fmas_f32 v3, v13, v10, v11
	v_div_fixup_f32 v1, v3, v1, 1.0
	v_fmaak_f32 v1, v1, v15, 0xbc23d70a
	v_add_f32_e32 v2, 1.0, v2
	v_div_scale_f32 v3, s[0:1], v2, v2, 1.0
	v_rcp_f32_e32 v4, v3
	v_max_f32_e32 v1, 0, v1
	v_add_f32_e32 v1, v8, v1
	s_lshl_b32 s0, s42, 5
	v_fma_f32 v5, -v3, v4, 1.0
	v_fmac_f32_e32 v4, v5, v4
	v_div_scale_f32 v5, vcc, 1.0, v2, 1.0
	v_mul_f32_e32 v6, v5, v4
	v_fma_f32 v7, -v3, v6, v5
	v_fmac_f32_e32 v6, v7, v4
	v_fma_f32 v3, -v3, v6, v5
	v_div_fmas_f32 v3, v3, v4, v6
	v_div_fixup_f32 v2, v3, v2, 1.0
	v_fmac_f32_e32 v9, v2, v16
	v_max_f32_e32 v2, 0, v9
	v_add_f32_e32 v2, v1, v2
	v_mov_b32_e32 v1, 0x16800
	v_lshl_or_b32 v1, v0, 2, v1
	v_cmp_gt_u32_e32 vcc, s0, v0
	ds_write_b32 v1, v2
	s_waitcnt lgkmcnt(0)
	s_barrier
	s_and_saveexec_b64 s[0:1], vcc
	s_cbranch_execz .LBB1_57
	ds_read2st64_b32 v[2:3], v1 offset1:2
	ds_read2st64_b32 v[4:5], v1 offset0:4 offset1:6
	v_add_u32_e32 v0, s33, v0
	v_ashrrev_i32_e32 v1, 31, v0
	v_lshl_add_u64 v[6:7], v[0:1], 2, s[10:11]
	s_waitcnt lgkmcnt(1)
	v_add_f32_e32 v1, v2, v3
	s_waitcnt lgkmcnt(0)
	v_add_f32_e32 v1, v1, v4
	v_add_f32_e32 v1, v1, v5
	v_add_u32_e32 v0, 0x7d00, v0
	v_mul_f32_e32 v2, 0x3d4ccccd, v1
	v_ashrrev_i32_e32 v1, 31, v0
	v_lshl_add_u64 v[0:1], v[0:1], 2, s[10:11]
	global_store_dword v[6:7], v2, off
	global_store_dword v[0:1], v2, off
